# full stack + attention K/V staging: source-level vmcnt(0) in front of the compiler's counted vmcnt(3..0) ladder removed (both layers)
# baseline (speedup 1.0000x reference)
.LBB0_969:
	s_and_b32 s15, s13, 1
	s_add_i32 s14, s13, 1
	s_cmp_ge_i32 s14, s87
	s_waitcnt lgkmcnt(0)
	s_barrier
	s_cbranch_scc1 .LBB0_980
	s_lshl_b32 s0, s15, 14
	s_xor_b32 s0, s0, 0x4000
	s_add_i32 s0, s0, 0
	v_add_u32_e32 v2, s0, v193
	s_waitcnt vmcnt(3)
	ds_write_b128 v2, v[166:169]
	v_add_u32_e32 v2, s0, v194
	s_waitcnt vmcnt(2)
	ds_write_b128 v2, v[170:173]
	v_add_u32_e32 v2, s0, v195
	s_waitcnt vmcnt(1)
	ds_write_b128 v2, v[174:177] offset:32768
	v_add_u32_e32 v2, s0, v196
	s_add_i32 s0, s13, 2
	s_cmp_ge_i32 s0, s87
	s_waitcnt vmcnt(0)
	ds_write_b128 v2, v[178:181] offset:32768
	s_cbranch_scc1 .LBB0_980
	s_cmp_gt_u32 s13, 1
	s_mov_b64 s[2:3], -1
	s_cbranch_scc0 .LBB0_977
	s_and_b64 vcc, exec, s[76:77]
	s_cbranch_vccz .LBB0_974
	v_readlane_b32 s0, v251, 42
	s_add_u32 s0, s0, s94
	v_readlane_b32 s1, v251, 40
	s_addc_u32 s1, s1, s95
	s_mov_b64 s[2:3], 0

.LBB0_3014:
	s_and_b32 s11, s10, 1
	s_add_i32 s12, s10, 1
	s_cmp_ge_i32 s12, s89
	s_waitcnt lgkmcnt(0)
	s_barrier
	s_cbranch_scc1 .LBB0_3025
	s_lshl_b32 s0, s11, 14
	s_xor_b32 s0, s0, 0x4000
	s_add_i32 s0, s0, 0
	v_add_u32_e32 v2, s0, v196
	s_waitcnt vmcnt(3)
	ds_write_b128 v2, v[166:169]
	v_add_u32_e32 v2, s0, v197
	s_waitcnt vmcnt(2)
	ds_write_b128 v2, v[170:173]
	v_add_u32_e32 v2, s0, v193
	s_waitcnt vmcnt(1)
	ds_write_b128 v2, v[174:177] offset:32768
	v_add_u32_e32 v2, s0, v194
	s_add_i32 s0, s10, 2
	s_cmp_ge_i32 s0, s89
	s_waitcnt vmcnt(0)
	ds_write_b128 v2, v[178:181] offset:32768
	s_cbranch_scc1 .LBB0_3025
	s_cmp_gt_u32 s10, 1
	s_mov_b64 s[4:5], -1
	s_cbranch_scc0 .LBB0_3022
	s_mov_b64 s[74:75], -1
	s_and_b64 vcc, exec, s[80:81]
	s_cbranch_vccz .LBB0_3019
	v_readlane_b32 s0, v251, 36
	s_add_u32 s0, s0, s96
	v_readlane_b32 s1, v251, 50
	s_addc_u32 s1, s1, s97
	s_mov_b64 s[74:75], 0
